# expert-up GEMM first K-iteration peeled too (no accumulator zero-init in 5 GEMM loops)
# speedup vs baseline: 1.0183x; 1.0040x over previous
.LBB0_1088:
	s_waitcnt vmcnt(0)
	v_lshlrev_b32_e32 v0, 8, v171
	v_and_b32_e32 v0, 0xfffffc00, v0
	v_cmp_lt_i32_e32 vcc, -1, v171
	v_readlane_b32 s30, v254, 32
	v_mov_b32_e32 v173, v113
	v_cndmask_b32_e32 v0, 0, v0, vcc
	v_add_u32_e32 v167, v0, v191
	v_lshlrev_b32_e32 v0, 8, v195
	v_and_b32_e32 v0, 0xfffffc00, v0
	v_cmp_lt_i32_e32 vcc, -1, v195
	v_mov_b32_e32 v175, v113
	v_readlane_b32 s31, v254, 33
	v_cndmask_b32_e32 v0, 0, v0, vcc
	v_add_u32_e32 v220, v0, v192
	v_lshlrev_b32_e32 v0, 8, v215
	v_and_b32_e32 v0, 0xfffffc00, v0
	v_cmp_lt_i32_e32 vcc, -1, v215
	s_add_u32 s37, s40, 0x100
	v_cndmask_b32_e32 v0, 0, v0, vcc
	v_add_u32_e32 v221, v0, v191
	v_lshlrev_b32_e32 v0, 8, v216
	v_and_b32_e32 v0, 0xfffffc00, v0
	v_cmp_lt_i32_e32 vcc, -1, v216
	v_lshl_add_u64 v[176:177], s[30:31], 0, v[174:175]
	v_lshl_add_u64 v[178:179], s[30:31], 0, v[172:173]
	v_cndmask_b32_e32 v0, 0, v0, vcc
	v_add_u32_e32 v222, v0, v192
	s_addc_u32 s47, s41, 0
	s_mov_b32 s49, -2
	s_mov_b64 s[72:73], 0
	v_mov_b32_e32 v173, v168
	v_mov_b32_e32 v175, v170
	v_mov_b32_e32 v217, v172
	v_mov_b32_e32 v218, v174
	s_cmpk_eq_i32 s72, 0x300
	s_cselect_b64 s[40:41], -1, 0
	s_and_b64 s[30:31], s[70:71], s[40:41]
	s_andn2_b64 vcc, exec, s[30:31]
	s_cbranch_vccnz .Lpeel_up_body
	v_mov_b32_e32 v173, v167
	v_mov_b32_e32 v175, v220
	v_mov_b32_e32 v217, v221
	v_mov_b32_e32 v218, v222
.Lpeel_up_body:
	s_add_u32 s30, s94, s72
	s_addc_u32 s31, s95, s73
	s_add_u32 s45, s30, 0x28dd9100
	s_addc_u32 s55, s31, 0
	s_and_b64 s[30:31], s[40:41], exec
	s_cselect_b32 s77, s91, s55
	s_cselect_b32 s76, s90, s45
	s_add_u32 s45, s37, s72
	s_addc_u32 s55, s47, s73
	s_and_b64 s[30:31], s[40:41], exec
	s_cselect_b32 s75, s65, s55
	s_cselect_b32 s74, s64, s45
	s_add_i32 s55, 0, 0x10000
	s_add_i32 s58, 0, 0x14000
	v_add_u32_e32 v0, s55, v193
	v_add_u32_e32 v12, s58, v193
	ds_read_b128 v[16:19], v0
	ds_read_b128 v[20:23], v0 offset:1024
	ds_read_b128 v[24:27], v0 offset:2048
	ds_read_b128 v[28:31], v0 offset:3072
	ds_read_b128 v[0:3], v12
	ds_read_b128 v[4:7], v12 offset:1024
	ds_read_b128 v[8:11], v12 offset:2048
	ds_read_b128 v[12:15], v12 offset:3072
	v_lshl_add_u64 v[206:207], v[178:179], 0, s[72:73]
	s_add_i32 m0, s7, 0xc000
	ds_read_b128 v[180:183], v169
	ds_read_b128 v[184:187], v169 offset:1024
	ds_read_b128 v[224:227], v169 offset:2048
	ds_read_b128 v[228:231], v169 offset:3072
	ds_read_b128 v[232:235], v169 offset:4096
	ds_read_b128 v[236:239], v169 offset:5120
	ds_read_b128 v[240:243], v169 offset:6144
	ds_read_b128 v[244:247], v169 offset:7168
	global_load_lds_dwordx4 v[206:207], off
	v_lshl_add_u64 v[206:207], v[176:177], 0, s[72:73]
	s_add_i32 m0, s7, 0xe000
	s_nop 0
	global_load_lds_dwordx4 v[206:207], off
	s_waitcnt vmcnt(8)
	s_waitcnt lgkmcnt(0)
	s_barrier
	s_setprio 1
	s_waitcnt lgkmcnt(0)
	v_mfma_scale_f32_16x16x128_f8f6f4 v[158:161], v[16:23], v[180:187], 0, v200, v201 op_sel_hi:[0,0,0]
	v_mfma_scale_f32_16x16x128_f8f6f4 v[150:153], v[24:31], v[180:187], 0, v200, v201 op_sel_hi:[0,0,0]
	v_mfma_scale_f32_16x16x128_f8f6f4 v[142:145], v[16:23], v[224:231], 0, v200, v201 op_sel_hi:[0,0,0]
	v_mfma_scale_f32_16x16x128_f8f6f4 v[134:137], v[24:31], v[224:231], 0, v200, v201 op_sel_hi:[0,0,0]
	v_mfma_scale_f32_16x16x128_f8f6f4 v[126:129], v[16:23], v[232:239], 0, v200, v201 op_sel_hi:[0,0,0]
	v_mfma_scale_f32_16x16x128_f8f6f4 v[118:121], v[24:31], v[232:239], 0, v200, v201 op_sel_hi:[0,0,0]
	v_mfma_scale_f32_16x16x128_f8f6f4 v[108:111], v[16:23], v[240:247], 0, v200, v201 op_sel_hi:[0,0,0]
	v_mfma_scale_f32_16x16x128_f8f6f4 v[100:103], v[24:31], v[240:247], 0, v200, v201 op_sel_hi:[0,0,0]
	s_setprio 0
	s_setprio 1
	v_mfma_scale_f32_16x16x128_f8f6f4 v[154:157], v[0:7], v[180:187], 0, v200, v201 op_sel_hi:[0,0,0]
	v_mfma_scale_f32_16x16x128_f8f6f4 v[146:149], v[8:15], v[180:187], 0, v200, v201 op_sel_hi:[0,0,0]
	v_mfma_scale_f32_16x16x128_f8f6f4 v[138:141], v[0:7], v[224:231], 0, v200, v201 op_sel_hi:[0,0,0]
	v_mfma_scale_f32_16x16x128_f8f6f4 v[130:133], v[8:15], v[224:231], 0, v200, v201 op_sel_hi:[0,0,0]
	v_mfma_scale_f32_16x16x128_f8f6f4 v[122:125], v[0:7], v[232:239], 0, v200, v201 op_sel_hi:[0,0,0]
	v_mfma_scale_f32_16x16x128_f8f6f4 v[114:117], v[8:15], v[232:239], 0, v200, v201 op_sel_hi:[0,0,0]
	v_mfma_scale_f32_16x16x128_f8f6f4 v[104:107], v[0:7], v[240:247], 0, v200, v201 op_sel_hi:[0,0,0]
	v_mfma_scale_f32_16x16x128_f8f6f4 v[96:99], v[8:15], v[240:247], 0, v200, v201 op_sel_hi:[0,0,0]
	s_setprio 0
	s_barrier
	s_add_i32 s30, s55, s14
	v_lshl_add_u64 v[180:181], s[74:75], 0, v[164:165]
	s_mov_b32 m0, s30
	ds_read_b128 v[224:227], v169 offset:16384
	ds_read_b128 v[228:231], v169 offset:17408
	ds_read_b128 v[232:235], v169 offset:18432
	ds_read_b128 v[236:239], v169 offset:19456
	ds_read_b128 v[240:243], v169 offset:20480
	ds_read_b128 v[244:247], v169 offset:21504
	ds_read_b128 v[206:209], v169 offset:22528
	ds_read_b128 v[210:213], v169 offset:23552
	global_load_lds_dwordx4 v[180:181], off
	s_add_i32 m0, s30, 0x2000
	s_add_u32 s30, s74, 0x20000
	v_lshl_add_u64 v[182:183], s[74:75], 0, v[162:163]
	s_addc_u32 s31, s75, 0
	s_add_i32 s45, s58, s14
	global_load_lds_dwordx4 v[182:183], off
	v_lshl_add_u64 v[184:185], s[30:31], 0, v[164:165]
	s_mov_b32 m0, s45
	v_cndmask_b32_e64 v112, v168, v173, s[40:41]
	global_load_lds_dwordx4 v[184:185], off
	v_lshl_add_u64 v[184:185], s[30:31], 0, v[162:163]
	s_add_i32 m0, s45, 0x2000
	s_nop 0
	global_load_lds_dwordx4 v[184:185], off
	s_mov_b32 m0, s7
	v_lshl_add_u64 v[184:185], s[76:77], 0, v[112:113]
	global_load_lds_dwordx4 v112, s[76:77]
	v_cndmask_b32_e64 v112, v170, v175, s[40:41]
	s_mov_b32 m0, s33
	v_lshl_add_u64 v[186:187], s[76:77], 0, v[112:113]
	global_load_lds_dwordx4 v112, s[76:77]
	s_waitcnt vmcnt(8)
	s_waitcnt lgkmcnt(0)
	s_barrier
	s_setprio 1
	s_waitcnt lgkmcnt(0)
	v_mfma_scale_f32_16x16x128_f8f6f4 v[92:95], v[16:23], v[224:231], 0, v200, v201 op_sel_hi:[0,0,0]
	v_mfma_scale_f32_16x16x128_f8f6f4 v[84:87], v[24:31], v[224:231], 0, v200, v201 op_sel_hi:[0,0,0]
	v_mfma_scale_f32_16x16x128_f8f6f4 v[76:79], v[16:23], v[232:239], 0, v200, v201 op_sel_hi:[0,0,0]
	v_mfma_scale_f32_16x16x128_f8f6f4 v[68:71], v[24:31], v[232:239], 0, v200, v201 op_sel_hi:[0,0,0]
	v_mfma_scale_f32_16x16x128_f8f6f4 v[60:63], v[16:23], v[240:247], 0, v200, v201 op_sel_hi:[0,0,0]
	v_mfma_scale_f32_16x16x128_f8f6f4 v[52:55], v[24:31], v[240:247], 0, v200, v201 op_sel_hi:[0,0,0]
	v_mfma_scale_f32_16x16x128_f8f6f4 v[44:47], v[16:23], v[206:213], 0, v200, v201 op_sel_hi:[0,0,0]
	v_mfma_scale_f32_16x16x128_f8f6f4 v[36:39], v[24:31], v[206:213], 0, v200, v201 op_sel_hi:[0,0,0]
	s_setprio 0
	s_setprio 1
	v_mfma_scale_f32_16x16x128_f8f6f4 v[88:91], v[0:7], v[224:231], 0, v200, v201 op_sel_hi:[0,0,0]
	v_mfma_scale_f32_16x16x128_f8f6f4 v[80:83], v[8:15], v[224:231], 0, v200, v201 op_sel_hi:[0,0,0]
	v_mfma_scale_f32_16x16x128_f8f6f4 v[72:75], v[0:7], v[232:239], 0, v200, v201 op_sel_hi:[0,0,0]
	v_mfma_scale_f32_16x16x128_f8f6f4 v[64:67], v[8:15], v[232:239], 0, v200, v201 op_sel_hi:[0,0,0]
	v_mfma_scale_f32_16x16x128_f8f6f4 v[56:59], v[0:7], v[240:247], 0, v200, v201 op_sel_hi:[0,0,0]
	v_mfma_scale_f32_16x16x128_f8f6f4 v[48:51], v[8:15], v[240:247], 0, v200, v201 op_sel_hi:[0,0,0]
	v_mfma_scale_f32_16x16x128_f8f6f4 v[40:43], v[0:7], v[206:213], 0, v200, v201 op_sel_hi:[0,0,0]
	v_mfma_scale_f32_16x16x128_f8f6f4 v[32:35], v[8:15], v[206:213], 0, v200, v201 op_sel_hi:[0,0,0]
	s_setprio 0
	s_barrier
	s_add_i32 s30, 0, 0x18000
	s_add_i32 s45, 0, 0x1c000
	v_add_u32_e32 v12, s30, v193
	v_add_u32_e32 v28, s45, v193
	ds_read_b128 v[0:3], v12
	ds_read_b128 v[4:7], v12 offset:1024
	ds_read_b128 v[8:11], v12 offset:2048
	ds_read_b128 v[12:15], v12 offset:3072
	ds_read_b128 v[16:19], v28
	ds_read_b128 v[20:23], v28 offset:1024
	ds_read_b128 v[24:27], v28 offset:2048
	ds_read_b128 v[28:31], v28 offset:3072
	s_mov_b32 m0, s34
	v_cndmask_b32_e64 v112, v172, v217, s[40:41]
	ds_read_b128 v[206:209], v169 offset:32768
	ds_read_b128 v[210:213], v169 offset:33792
	ds_read_b128 v[224:227], v169 offset:34816
	ds_read_b128 v[228:231], v169 offset:35840
	ds_read_b128 v[232:235], v169 offset:36864
	ds_read_b128 v[236:239], v169 offset:37888
	ds_read_b128 v[240:243], v169 offset:38912
	ds_read_b128 v[244:247], v169 offset:39936
	global_load_lds_dwordx4 v112, s[76:77]
	v_cndmask_b32_e64 v112, v174, v218, s[40:41]
	s_mov_b32 m0, s50
	s_nop 0
	global_load_lds_dwordx4 v112, s[76:77]
	s_waitcnt vmcnt(8)
	s_waitcnt lgkmcnt(0)
	s_barrier
	s_setprio 1
	s_waitcnt lgkmcnt(0)
	v_mfma_scale_f32_16x16x128_f8f6f4 v[158:161], v[0:7], v[206:213], v[158:161], v200, v201 op_sel_hi:[0,0,0]
	v_mfma_scale_f32_16x16x128_f8f6f4 v[150:153], v[8:15], v[206:213], v[150:153], v200, v201 op_sel_hi:[0,0,0]
	v_mfma_scale_f32_16x16x128_f8f6f4 v[142:145], v[0:7], v[224:231], v[142:145], v200, v201 op_sel_hi:[0,0,0]
	v_mfma_scale_f32_16x16x128_f8f6f4 v[134:137], v[8:15], v[224:231], v[134:137], v200, v201 op_sel_hi:[0,0,0]
	v_mfma_scale_f32_16x16x128_f8f6f4 v[126:129], v[0:7], v[232:239], v[126:129], v200, v201 op_sel_hi:[0,0,0]
	v_mfma_scale_f32_16x16x128_f8f6f4 v[118:121], v[8:15], v[232:239], v[118:121], v200, v201 op_sel_hi:[0,0,0]
	v_mfma_scale_f32_16x16x128_f8f6f4 v[108:111], v[0:7], v[240:247], v[108:111], v200, v201 op_sel_hi:[0,0,0]
	v_mfma_scale_f32_16x16x128_f8f6f4 v[100:103], v[8:15], v[240:247], v[100:103], v200, v201 op_sel_hi:[0,0,0]
	s_setprio 0
	s_setprio 1
	v_mfma_scale_f32_16x16x128_f8f6f4 v[154:157], v[16:23], v[206:213], v[154:157], v200, v201 op_sel_hi:[0,0,0]
	v_mfma_scale_f32_16x16x128_f8f6f4 v[146:149], v[24:31], v[206:213], v[146:149], v200, v201 op_sel_hi:[0,0,0]
	v_mfma_scale_f32_16x16x128_f8f6f4 v[138:141], v[16:23], v[224:231], v[138:141], v200, v201 op_sel_hi:[0,0,0]
	v_mfma_scale_f32_16x16x128_f8f6f4 v[130:133], v[24:31], v[224:231], v[130:133], v200, v201 op_sel_hi:[0,0,0]
	v_mfma_scale_f32_16x16x128_f8f6f4 v[122:125], v[16:23], v[232:239], v[122:125], v200, v201 op_sel_hi:[0,0,0]
	v_mfma_scale_f32_16x16x128_f8f6f4 v[114:117], v[24:31], v[232:239], v[114:117], v200, v201 op_sel_hi:[0,0,0]
	v_mfma_scale_f32_16x16x128_f8f6f4 v[104:107], v[16:23], v[240:247], v[104:107], v200, v201 op_sel_hi:[0,0,0]
	v_mfma_scale_f32_16x16x128_f8f6f4 v[96:99], v[24:31], v[240:247], v[96:99], v200, v201 op_sel_hi:[0,0,0]
	s_setprio 0
	s_barrier
	s_add_i32 s30, s30, s14
	v_lshl_add_u64 v[180:181], v[180:181], 0, s[56:57]
	s_mov_b32 m0, s30
	ds_read_b128 v[206:209], v169 offset:49152
	ds_read_b128 v[210:213], v169 offset:50176
	ds_read_b128 v[224:227], v169 offset:51200
	ds_read_b128 v[228:231], v169 offset:52224
	ds_read_b128 v[232:235], v169 offset:53248
	ds_read_b128 v[236:239], v169 offset:54272
	ds_read_b128 v[240:243], v169 offset:55296
	ds_read_b128 v[244:247], v169 offset:56320
	global_load_lds_dwordx4 v[180:181], off
	s_add_i32 m0, s30, 0x2000
	s_add_u32 s30, s74, 0x20080
	v_lshl_add_u64 v[180:181], v[182:183], 0, s[56:57]
	s_addc_u32 s31, s75, 0
	s_add_i32 s40, s45, s14
	global_load_lds_dwordx4 v[180:181], off
	v_lshl_add_u64 v[180:181], s[30:31], 0, v[164:165]
	s_mov_b32 m0, s40
	s_nop 0
	global_load_lds_dwordx4 v[180:181], off
	v_lshl_add_u64 v[180:181], s[30:31], 0, v[162:163]
	s_add_i32 m0, s40, 0x2000
	s_nop 0
	global_load_lds_dwordx4 v[180:181], off
	v_lshl_add_u64 v[180:181], v[184:185], 0, s[56:57]
	s_mov_b32 m0, s4
	s_nop 0
	global_load_lds_dwordx4 v[180:181], off
	v_lshl_add_u64 v[180:181], v[186:187], 0, s[56:57]
	s_mov_b32 m0, s51
	s_nop 0
	global_load_lds_dwordx4 v[180:181], off
	s_waitcnt vmcnt(8)
	s_waitcnt lgkmcnt(0)
	s_barrier
	s_setprio 1
	s_waitcnt lgkmcnt(0)
	v_mfma_scale_f32_16x16x128_f8f6f4 v[92:95], v[0:7], v[206:213], v[92:95], v200, v201 op_sel_hi:[0,0,0]
	v_mfma_scale_f32_16x16x128_f8f6f4 v[84:87], v[8:15], v[206:213], v[84:87], v200, v201 op_sel_hi:[0,0,0]
	v_mfma_scale_f32_16x16x128_f8f6f4 v[76:79], v[0:7], v[224:231], v[76:79], v200, v201 op_sel_hi:[0,0,0]
	v_mfma_scale_f32_16x16x128_f8f6f4 v[68:71], v[8:15], v[224:231], v[68:71], v200, v201 op_sel_hi:[0,0,0]
	v_mfma_scale_f32_16x16x128_f8f6f4 v[60:63], v[0:7], v[232:239], v[60:63], v200, v201 op_sel_hi:[0,0,0]
	v_mfma_scale_f32_16x16x128_f8f6f4 v[52:55], v[8:15], v[232:239], v[52:55], v200, v201 op_sel_hi:[0,0,0]
	v_mfma_scale_f32_16x16x128_f8f6f4 v[44:47], v[0:7], v[240:247], v[44:47], v200, v201 op_sel_hi:[0,0,0]
	v_mfma_scale_f32_16x16x128_f8f6f4 v[36:39], v[8:15], v[240:247], v[36:39], v200, v201 op_sel_hi:[0,0,0]
	s_setprio 0
	s_setprio 1
	v_mfma_scale_f32_16x16x128_f8f6f4 v[88:91], v[16:23], v[206:213], v[88:91], v200, v201 op_sel_hi:[0,0,0]
	v_mfma_scale_f32_16x16x128_f8f6f4 v[80:83], v[24:31], v[206:213], v[80:83], v200, v201 op_sel_hi:[0,0,0]
	v_mfma_scale_f32_16x16x128_f8f6f4 v[72:75], v[16:23], v[224:231], v[72:75], v200, v201 op_sel_hi:[0,0,0]
	v_mfma_scale_f32_16x16x128_f8f6f4 v[64:67], v[24:31], v[224:231], v[64:67], v200, v201 op_sel_hi:[0,0,0]
	v_mfma_scale_f32_16x16x128_f8f6f4 v[56:59], v[16:23], v[232:239], v[56:59], v200, v201 op_sel_hi:[0,0,0]
	v_mfma_scale_f32_16x16x128_f8f6f4 v[48:51], v[24:31], v[232:239], v[48:51], v200, v201 op_sel_hi:[0,0,0]
	v_mfma_scale_f32_16x16x128_f8f6f4 v[40:43], v[16:23], v[240:247], v[40:43], v200, v201 op_sel_hi:[0,0,0]
	v_mfma_scale_f32_16x16x128_f8f6f4 v[32:35], v[24:31], v[240:247], v[32:35], v200, v201 op_sel_hi:[0,0,0]
	s_setprio 0
	s_barrier
	s_add_i32 s49, s49, 2
	s_add_u32 s72, s72, 0x100
	s_addc_u32 s73, s73, 0
	s_cmp_gt_u32 s49, 5
	s_cbranch_scc1 .LBB0_1092
	s_branch .LBB0_1090
